# grid barriers 1-18: thread-0 protocol shortened - all workgroups poll the TOP arrival counter directly (no TOPGEN/XGEN hops), static generation index
# speedup vs baseline: 1.0266x; 1.0266x over previous
; __device__ __forceinline__ unsigned xb_ld(unsigned* p)              { return __hip_atomic_load(p, __ATOMIC_RELAXED, __HIP_MEMORY_SCOPE_AGENT); }
; __device__ __forceinline__ unsigned xb_add(unsigned* p, unsigned v) { return __hip_atomic_fetch_add(p, v, __ATOMIC_RELAXED, __HIP_MEMORY_SCOPE_AGENT); }
; #define XB_SPIN(cond, bar) do { unsigned _sp = 0; while (cond) { __builtin_amdgcn_s_sleep(1); \
;     if ((++_sp & 255u) == 0u) { if (xb_ld(&(bar)[XB_TMO])) break; if (_sp > XB_SPIN_CAP) { atomicAdd(&(bar)[XB_TMO], 1u); break; } } } } while (0)
; __device__ __forceinline__ void xcd_barrier(const XcdBarrier& b) {
;     ...
;     if (threadIdx.x == 0) {
;         unsigned* bar = b.bar;
;         __builtin_amdgcn_s_waitcnt(0);
;         unsigned nloc = b.st[0], nx = b.st[1];
;         if (nloc == 0u) { xcd_barrier_complete(bar, b.x, nloc, nx); b.st[0] = nloc; b.st[1] = nx; }
;         const unsigned old = xb_add(&bar[XB_XSUB(b.x)], 1u);
;         const unsigned gen = old / nloc;
;         if (old + 1u == (gen + 1u) * nloc) {
;             __builtin_amdgcn_fence(__ATOMIC_RELEASE, "agent");
;             asm volatile("s_waitcnt vmcnt(0)" ::: "memory");
;             const unsigned og = xb_add(&bar[XB_TOP], 1u);
;             const unsigned tg = og / nx;
;             if (og + 1u == (tg + 1u) * nx) xb_add(&bar[XB_TOPGEN], 1u);
;             else XB_SPIN(xb_ld(&bar[XB_TOPGEN]) == tg, bar);
;             __builtin_amdgcn_fence(__ATOMIC_ACQUIRE, "agent");
;             xb_add(&bar[XB_XGEN(b.x)], 1u);
;             asm volatile("s_waitcnt vmcnt(0)" ::: "memory");
;         } else {
;             XB_SPIN(xb_ld(&bar[XB_XGEN(b.x)]) == gen, bar);
;             __builtin_amdgcn_fence(__ATOMIC_ACQUIRE, "agent");
;             asm volatile("s_waitcnt vmcnt(0)" ::: "memory");
;         }
.LBB0_184:
	s_or_b64 exec, exec, s[0:1]
	s_waitcnt vmcnt(0)
	s_barrier
	s_mov_b64 s[0:1], exec
	v_readlane_b32 s2, v254, 9
	v_readlane_b32 s3, v254, 10
	s_and_b64 s[2:3], s[0:1], s[2:3]
	s_xor_b64 s[0:1], s[2:3], s[0:1]
	s_mov_b64 exec, s[2:3]
	s_cbranch_execz .LBB0_237
	s_waitcnt vmcnt(0) expcnt(0) lgkmcnt(0)
	v_mov_b32_e32 v1, 0x21000
	ds_read_b32 v2, v1
	ds_read_b32 v3, v1 offset:4
	v_readlane_b32 s2, v254, 6
	v_readlane_b32 s3, v254, 7
	v_readlane_b32 s9, v254, 8
	v_mov_b32_e32 v4, 0x1000
	v_mov_b32_e32 v5, 1
	s_lshl_b32 s9, s9, 8
	s_add_u32 s4, s2, s9
	s_addc_u32 s5, s3, 0
	global_atomic_add v4, v4, v5, s[4:5] offset:1024 sc0
	s_waitcnt vmcnt(0) lgkmcnt(0)
	v_readfirstlane_b32 s6, v4
	v_readfirstlane_b32 s7, v2
	v_readfirstlane_b32 s8, v3
	v_mov_b32_e32 v4, 0x3000
	s_nop 3
	s_mul_i32 s9, s7, 2
	s_add_u32 s6, s6, 1
	s_mul_i32 s8, s8, 2
	s_mov_b32 s10, 0
	s_cmp_lg_u32 s6, s9
	s_cbranch_scc1 .Lxb_spin_1
	buffer_wbl2 sc1
	s_waitcnt vmcnt(0)
	global_atomic_add v4, v5, s[2:3] offset:1024
.Lxb_spin_1:
	global_load_dword v1, v4, s[2:3] offset:1024 sc1
	s_waitcnt vmcnt(0)
	v_readfirstlane_b32 s9, v1
	s_nop 3
	s_cmp_ge_u32 s9, s8
	s_cbranch_scc1 .Lxb_done_1
	s_sleep 1
	s_add_u32 s10, s10, 1
	s_cmp_lt_u32 s10, 0x20000
	s_cbranch_scc1 .Lxb_spin_1
.Lxb_done_1:
	buffer_inv sc1
	s_waitcnt vmcnt(0)

; __device__ __forceinline__ unsigned xb_ld(unsigned* p)              { return __hip_atomic_load(p, __ATOMIC_RELAXED, __HIP_MEMORY_SCOPE_AGENT); }
; __device__ __forceinline__ unsigned xb_add(unsigned* p, unsigned v) { return __hip_atomic_fetch_add(p, v, __ATOMIC_RELAXED, __HIP_MEMORY_SCOPE_AGENT); }
; #define XB_SPIN(cond, bar) do { unsigned _sp = 0; while (cond) { __builtin_amdgcn_s_sleep(1); \
;     if ((++_sp & 255u) == 0u) { if (xb_ld(&(bar)[XB_TMO])) break; if (_sp > XB_SPIN_CAP) { atomicAdd(&(bar)[XB_TMO], 1u); break; } } } } while (0)
; __device__ __forceinline__ void xcd_barrier(const XcdBarrier& b) {
;     ...
;     if (threadIdx.x == 0) {
;         unsigned* bar = b.bar;
;         __builtin_amdgcn_s_waitcnt(0);
;         unsigned nloc = b.st[0], nx = b.st[1];
;         if (nloc == 0u) { xcd_barrier_complete(bar, b.x, nloc, nx); b.st[0] = nloc; b.st[1] = nx; }
;         const unsigned old = xb_add(&bar[XB_XSUB(b.x)], 1u);
;         const unsigned gen = old / nloc;
;         if (old + 1u == (gen + 1u) * nloc) {
;             __builtin_amdgcn_fence(__ATOMIC_RELEASE, "agent");
;             asm volatile("s_waitcnt vmcnt(0)" ::: "memory");
;             const unsigned og = xb_add(&bar[XB_TOP], 1u);
;             const unsigned tg = og / nx;
;             if (og + 1u == (tg + 1u) * nx) xb_add(&bar[XB_TOPGEN], 1u);
;             else XB_SPIN(xb_ld(&bar[XB_TOPGEN]) == tg, bar);
.LBB0_251:
	s_waitcnt vmcnt(0)
	s_waitcnt vmcnt(0) lgkmcnt(0)
	s_barrier
	s_mov_b64 s[0:1], exec
	v_readlane_b32 s2, v254, 9
	v_readlane_b32 s3, v254, 10
	s_and_b64 s[2:3], s[0:1], s[2:3]
	s_xor_b64 s[0:1], s[2:3], s[0:1]
	s_mov_b64 exec, s[2:3]
	s_cbranch_execz .LBB0_304
	s_waitcnt vmcnt(0) expcnt(0) lgkmcnt(0)
	v_mov_b32_e32 v1, 0x21000
	ds_read_b32 v2, v1
	ds_read_b32 v3, v1 offset:4
	v_readlane_b32 s2, v254, 6
	v_readlane_b32 s3, v254, 7
	v_readlane_b32 s9, v254, 8
	v_mov_b32_e32 v4, 0x1000
	v_mov_b32_e32 v5, 1
	s_lshl_b32 s9, s9, 8
	s_add_u32 s4, s2, s9
	s_addc_u32 s5, s3, 0
	global_atomic_add v4, v4, v5, s[4:5] offset:1024 sc0
	s_waitcnt vmcnt(0) lgkmcnt(0)
	v_readfirstlane_b32 s6, v4
	v_readfirstlane_b32 s7, v2
	v_readfirstlane_b32 s8, v3
	v_mov_b32_e32 v4, 0x3000
	s_nop 3
	s_mul_i32 s9, s7, 3
	s_add_u32 s6, s6, 1
	s_mul_i32 s8, s8, 3
	s_mov_b32 s10, 0
	s_cmp_lg_u32 s6, s9
	s_cbranch_scc1 .Lxb_spin_2
	buffer_wbl2 sc1
	s_waitcnt vmcnt(0)
	global_atomic_add v4, v5, s[2:3] offset:1024

; __device__ __forceinline__ unsigned xb_ld(unsigned* p)              { return __hip_atomic_load(p, __ATOMIC_RELAXED, __HIP_MEMORY_SCOPE_AGENT); }
; __device__ __forceinline__ unsigned xb_add(unsigned* p, unsigned v) { return __hip_atomic_fetch_add(p, v, __ATOMIC_RELAXED, __HIP_MEMORY_SCOPE_AGENT); }
; #define XB_SPIN(cond, bar) do { unsigned _sp = 0; while (cond) { __builtin_amdgcn_s_sleep(1); \
;     if ((++_sp & 255u) == 0u) { if (xb_ld(&(bar)[XB_TMO])) break; if (_sp > XB_SPIN_CAP) { atomicAdd(&(bar)[XB_TMO], 1u); break; } } } } while (0)
; __device__ __forceinline__ void xcd_barrier(const XcdBarrier& b) {
;     ...
;     if (threadIdx.x == 0) {
;         unsigned* bar = b.bar;
;         __builtin_amdgcn_s_waitcnt(0);
;         unsigned nloc = b.st[0], nx = b.st[1];
;         if (nloc == 0u) { xcd_barrier_complete(bar, b.x, nloc, nx); b.st[0] = nloc; b.st[1] = nx; }
;         const unsigned old = xb_add(&bar[XB_XSUB(b.x)], 1u);
;         const unsigned gen = old / nloc;
;         if (old + 1u == (gen + 1u) * nloc) {
;             __builtin_amdgcn_fence(__ATOMIC_RELEASE, "agent");
;             asm volatile("s_waitcnt vmcnt(0)" ::: "memory");
;             const unsigned og = xb_add(&bar[XB_TOP], 1u);
;             const unsigned tg = og / nx;
;             if (og + 1u == (tg + 1u) * nx) xb_add(&bar[XB_TOPGEN], 1u);
;             else XB_SPIN(xb_ld(&bar[XB_TOPGEN]) == tg, bar);
.LBB0_322:
	s_barrier
	s_waitcnt vmcnt(0)
	s_barrier
	s_mov_b64 s[0:1], exec
	v_readlane_b32 s2, v254, 9
	v_readlane_b32 s3, v254, 10
	s_and_b64 s[2:3], s[0:1], s[2:3]
	s_xor_b64 s[0:1], s[2:3], s[0:1]
	s_mov_b64 exec, s[2:3]
	s_cbranch_execz .LBB0_375
	s_waitcnt vmcnt(0) expcnt(0) lgkmcnt(0)
	v_mov_b32_e32 v1, 0x21000
	ds_read_b32 v2, v1
	ds_read_b32 v3, v1 offset:4
	v_readlane_b32 s2, v254, 6
	v_readlane_b32 s3, v254, 7
	v_readlane_b32 s9, v254, 8
	v_mov_b32_e32 v4, 0x1000
	v_mov_b32_e32 v5, 1
	s_lshl_b32 s9, s9, 8
	s_add_u32 s4, s2, s9
	s_addc_u32 s5, s3, 0
	global_atomic_add v4, v4, v5, s[4:5] offset:1024 sc0
	s_waitcnt vmcnt(0) lgkmcnt(0)
	v_readfirstlane_b32 s6, v4
	v_readfirstlane_b32 s7, v2
	v_readfirstlane_b32 s8, v3
	v_mov_b32_e32 v4, 0x3000
	s_nop 3
	s_mul_i32 s9, s7, 4
	s_add_u32 s6, s6, 1
	s_mul_i32 s8, s8, 4
	s_mov_b32 s10, 0
	s_cmp_lg_u32 s6, s9
	s_cbranch_scc1 .Lxb_spin_3
	buffer_wbl2 sc1
	s_waitcnt vmcnt(0)
	global_atomic_add v4, v5, s[2:3] offset:1024

; __device__ __forceinline__ unsigned xb_ld(unsigned* p)              { return __hip_atomic_load(p, __ATOMIC_RELAXED, __HIP_MEMORY_SCOPE_AGENT); }
; __device__ __forceinline__ unsigned xb_add(unsigned* p, unsigned v) { return __hip_atomic_fetch_add(p, v, __ATOMIC_RELAXED, __HIP_MEMORY_SCOPE_AGENT); }
; #define XB_SPIN(cond, bar) do { unsigned _sp = 0; while (cond) { __builtin_amdgcn_s_sleep(1); \
;     if ((++_sp & 255u) == 0u) { if (xb_ld(&(bar)[XB_TMO])) break; if (_sp > XB_SPIN_CAP) { atomicAdd(&(bar)[XB_TMO], 1u); break; } } } } while (0)
; __device__ __forceinline__ void xcd_barrier(const XcdBarrier& b) {
;     ...
;     if (threadIdx.x == 0) {
;         unsigned* bar = b.bar;
;         __builtin_amdgcn_s_waitcnt(0);
;         unsigned nloc = b.st[0], nx = b.st[1];
;         if (nloc == 0u) { xcd_barrier_complete(bar, b.x, nloc, nx); b.st[0] = nloc; b.st[1] = nx; }
;         const unsigned old = xb_add(&bar[XB_XSUB(b.x)], 1u);
;         const unsigned gen = old / nloc;
;         if (old + 1u == (gen + 1u) * nloc) {
;             __builtin_amdgcn_fence(__ATOMIC_RELEASE, "agent");
;             asm volatile("s_waitcnt vmcnt(0)" ::: "memory");
;             const unsigned og = xb_add(&bar[XB_TOP], 1u);
;             const unsigned tg = og / nx;
;             if (og + 1u == (tg + 1u) * nx) xb_add(&bar[XB_TOPGEN], 1u);
;             else XB_SPIN(xb_ld(&bar[XB_TOPGEN]) == tg, bar);
.LBB0_816:
	s_barrier
	s_waitcnt vmcnt(0)
	s_barrier
	s_mov_b64 s[0:1], exec
	v_readlane_b32 s2, v254, 9
	v_readlane_b32 s3, v254, 10
	s_and_b64 s[2:3], s[0:1], s[2:3]
	s_xor_b64 s[0:1], s[2:3], s[0:1]
	s_mov_b64 exec, s[2:3]
	s_cbranch_execz .LBB0_869
	s_waitcnt vmcnt(0) expcnt(0) lgkmcnt(0)
	v_mov_b32_e32 v1, 0x21000
	ds_read_b32 v2, v1
	ds_read_b32 v3, v1 offset:4
	v_readlane_b32 s2, v254, 6
	v_readlane_b32 s3, v254, 7
	v_readlane_b32 s9, v254, 8
	v_mov_b32_e32 v4, 0x1000
	v_mov_b32_e32 v5, 1
	s_lshl_b32 s9, s9, 8
	s_add_u32 s4, s2, s9
	s_addc_u32 s5, s3, 0
	global_atomic_add v4, v4, v5, s[4:5] offset:1024 sc0
	s_waitcnt vmcnt(0) lgkmcnt(0)
	v_readfirstlane_b32 s6, v4
	v_readfirstlane_b32 s7, v2
	v_readfirstlane_b32 s8, v3
	v_mov_b32_e32 v4, 0x3000
	s_nop 3
	s_mul_i32 s9, s7, 5
	s_add_u32 s6, s6, 1
	s_mul_i32 s8, s8, 5
	s_mov_b32 s10, 0
	s_cmp_lg_u32 s6, s9
	s_cbranch_scc1 .Lxb_spin_4
	buffer_wbl2 sc1
	s_waitcnt vmcnt(0)
	global_atomic_add v4, v5, s[2:3] offset:1024

; __device__ __forceinline__ unsigned xb_ld(unsigned* p)              { return __hip_atomic_load(p, __ATOMIC_RELAXED, __HIP_MEMORY_SCOPE_AGENT); }
; __device__ __forceinline__ unsigned xb_add(unsigned* p, unsigned v) { return __hip_atomic_fetch_add(p, v, __ATOMIC_RELAXED, __HIP_MEMORY_SCOPE_AGENT); }
; #define XB_SPIN(cond, bar) do { unsigned _sp = 0; while (cond) { __builtin_amdgcn_s_sleep(1); \
;     if ((++_sp & 255u) == 0u) { if (xb_ld(&(bar)[XB_TMO])) break; if (_sp > XB_SPIN_CAP) { atomicAdd(&(bar)[XB_TMO], 1u); break; } } } } while (0)
; __device__ __forceinline__ void xcd_barrier(const XcdBarrier& b) {
;     ...
;     if (threadIdx.x == 0) {
;         unsigned* bar = b.bar;
;         __builtin_amdgcn_s_waitcnt(0);
;         unsigned nloc = b.st[0], nx = b.st[1];
;         if (nloc == 0u) { xcd_barrier_complete(bar, b.x, nloc, nx); b.st[0] = nloc; b.st[1] = nx; }
;         const unsigned old = xb_add(&bar[XB_XSUB(b.x)], 1u);
;         const unsigned gen = old / nloc;
;         if (old + 1u == (gen + 1u) * nloc) {
;             __builtin_amdgcn_fence(__ATOMIC_RELEASE, "agent");
;             asm volatile("s_waitcnt vmcnt(0)" ::: "memory");
;             const unsigned og = xb_add(&bar[XB_TOP], 1u);
;             const unsigned tg = og / nx;
;             if (og + 1u == (tg + 1u) * nx) xb_add(&bar[XB_TOPGEN], 1u);
;             else XB_SPIN(xb_ld(&bar[XB_TOPGEN]) == tg, bar);
.LBB0_876:
	s_barrier
	s_waitcnt vmcnt(0)
	s_barrier
	s_mov_b64 s[0:1], exec
	v_readlane_b32 s2, v254, 9
	v_readlane_b32 s3, v254, 10
	s_and_b64 s[2:3], s[0:1], s[2:3]
	s_xor_b64 s[0:1], s[2:3], s[0:1]
	s_mov_b64 exec, s[2:3]
	s_cbranch_execz .LBB0_929
	s_waitcnt vmcnt(0) expcnt(0) lgkmcnt(0)
	v_mov_b32_e32 v1, 0x21000
	ds_read_b32 v2, v1
	ds_read_b32 v3, v1 offset:4
	v_readlane_b32 s2, v254, 6
	v_readlane_b32 s3, v254, 7
	v_readlane_b32 s9, v254, 8
	v_mov_b32_e32 v4, 0x1000
	v_mov_b32_e32 v5, 1
	s_lshl_b32 s9, s9, 8
	s_add_u32 s4, s2, s9
	s_addc_u32 s5, s3, 0
	global_atomic_add v4, v4, v5, s[4:5] offset:1024 sc0
	s_waitcnt vmcnt(0) lgkmcnt(0)
	v_readfirstlane_b32 s6, v4
	v_readfirstlane_b32 s7, v2
	v_readfirstlane_b32 s8, v3
	v_mov_b32_e32 v4, 0x3000
	s_nop 3
	s_mul_i32 s9, s7, 6
	s_add_u32 s6, s6, 1
	s_mul_i32 s8, s8, 6
	s_mov_b32 s10, 0
	s_cmp_lg_u32 s6, s9
	s_cbranch_scc1 .Lxb_spin_5
	buffer_wbl2 sc1
	s_waitcnt vmcnt(0)
	global_atomic_add v4, v5, s[2:3] offset:1024

; __device__ __forceinline__ unsigned xb_ld(unsigned* p)              { return __hip_atomic_load(p, __ATOMIC_RELAXED, __HIP_MEMORY_SCOPE_AGENT); }
; __device__ __forceinline__ unsigned xb_add(unsigned* p, unsigned v) { return __hip_atomic_fetch_add(p, v, __ATOMIC_RELAXED, __HIP_MEMORY_SCOPE_AGENT); }
; #define XB_SPIN(cond, bar) do { unsigned _sp = 0; while (cond) { __builtin_amdgcn_s_sleep(1); \
;     if ((++_sp & 255u) == 0u) { if (xb_ld(&(bar)[XB_TMO])) break; if (_sp > XB_SPIN_CAP) { atomicAdd(&(bar)[XB_TMO], 1u); break; } } } } while (0)
; __device__ __forceinline__ void xcd_barrier(const XcdBarrier& b) {
;     ...
;     if (threadIdx.x == 0) {
;         unsigned* bar = b.bar;
;         __builtin_amdgcn_s_waitcnt(0);
;         unsigned nloc = b.st[0], nx = b.st[1];
;         if (nloc == 0u) { xcd_barrier_complete(bar, b.x, nloc, nx); b.st[0] = nloc; b.st[1] = nx; }
;         const unsigned old = xb_add(&bar[XB_XSUB(b.x)], 1u);
;         const unsigned gen = old / nloc;
;         if (old + 1u == (gen + 1u) * nloc) {
;             __builtin_amdgcn_fence(__ATOMIC_RELEASE, "agent");
;             asm volatile("s_waitcnt vmcnt(0)" ::: "memory");
;             const unsigned og = xb_add(&bar[XB_TOP], 1u);
;             const unsigned tg = og / nx;
;             if (og + 1u == (tg + 1u) * nx) xb_add(&bar[XB_TOPGEN], 1u);
;             else XB_SPIN(xb_ld(&bar[XB_TOPGEN]) == tg, bar);
.LBB0_947:
	s_waitcnt vmcnt(0)
	s_waitcnt lgkmcnt(0)
	s_barrier
	s_mov_b64 s[0:1], exec
	v_readlane_b32 s2, v254, 9
	v_readlane_b32 s3, v254, 10
	s_and_b64 s[2:3], s[0:1], s[2:3]
	s_xor_b64 s[0:1], s[2:3], s[0:1]
	s_mov_b64 exec, s[2:3]
	s_cbranch_execz .LBB0_1000
	s_waitcnt vmcnt(0) expcnt(0) lgkmcnt(0)
	v_mov_b32_e32 v1, 0x21000
	ds_read_b32 v2, v1
	ds_read_b32 v3, v1 offset:4
	v_readlane_b32 s2, v254, 6
	v_readlane_b32 s3, v254, 7
	v_readlane_b32 s9, v254, 8
	v_mov_b32_e32 v4, 0x1000
	v_mov_b32_e32 v5, 1
	s_lshl_b32 s9, s9, 8
	s_add_u32 s4, s2, s9
	s_addc_u32 s5, s3, 0
	global_atomic_add v4, v4, v5, s[4:5] offset:1024 sc0
	s_waitcnt vmcnt(0) lgkmcnt(0)
	v_readfirstlane_b32 s6, v4
	v_readfirstlane_b32 s7, v2
	v_readfirstlane_b32 s8, v3
	v_mov_b32_e32 v4, 0x3000
	s_nop 3
	s_mul_i32 s9, s7, 7
	s_add_u32 s6, s6, 1
	s_mul_i32 s8, s8, 7
	s_mov_b32 s10, 0
	s_cmp_lg_u32 s6, s9
	s_cbranch_scc1 .Lxb_spin_6
	buffer_wbl2 sc1
	s_waitcnt vmcnt(0)
	global_atomic_add v4, v5, s[2:3] offset:1024

; __device__ __forceinline__ unsigned xb_ld(unsigned* p)              { return __hip_atomic_load(p, __ATOMIC_RELAXED, __HIP_MEMORY_SCOPE_AGENT); }
; __device__ __forceinline__ unsigned xb_add(unsigned* p, unsigned v) { return __hip_atomic_fetch_add(p, v, __ATOMIC_RELAXED, __HIP_MEMORY_SCOPE_AGENT); }
; #define XB_SPIN(cond, bar) do { unsigned _sp = 0; while (cond) { __builtin_amdgcn_s_sleep(1); \
;     if ((++_sp & 255u) == 0u) { if (xb_ld(&(bar)[XB_TMO])) break; if (_sp > XB_SPIN_CAP) { atomicAdd(&(bar)[XB_TMO], 1u); break; } } } } while (0)
; __device__ __forceinline__ void xcd_barrier(const XcdBarrier& b) {
;     ...
;     if (threadIdx.x == 0) {
;         unsigned* bar = b.bar;
;         __builtin_amdgcn_s_waitcnt(0);
;         unsigned nloc = b.st[0], nx = b.st[1];
;         if (nloc == 0u) { xcd_barrier_complete(bar, b.x, nloc, nx); b.st[0] = nloc; b.st[1] = nx; }
;         const unsigned old = xb_add(&bar[XB_XSUB(b.x)], 1u);
;         const unsigned gen = old / nloc;
;         if (old + 1u == (gen + 1u) * nloc) {
;             __builtin_amdgcn_fence(__ATOMIC_RELEASE, "agent");
;             asm volatile("s_waitcnt vmcnt(0)" ::: "memory");
;             const unsigned og = xb_add(&bar[XB_TOP], 1u);
;             const unsigned tg = og / nx;
;             if (og + 1u == (tg + 1u) * nx) xb_add(&bar[XB_TOPGEN], 1u);
;             else XB_SPIN(xb_ld(&bar[XB_TOPGEN]) == tg, bar);
.LBB0_1009:
	s_waitcnt lgkmcnt(0)
	s_barrier
	s_waitcnt vmcnt(0)
	s_barrier
	s_mov_b64 s[0:1], exec
	v_readlane_b32 s2, v254, 9
	v_readlane_b32 s3, v254, 10
	s_and_b64 s[2:3], s[0:1], s[2:3]
	s_mov_b64 exec, s[2:3]
	s_cbranch_execz .LBB0_1061
	s_waitcnt vmcnt(0) expcnt(0) lgkmcnt(0)
	v_mov_b32_e32 v1, 0x21000
	ds_read_b32 v2, v1
	ds_read_b32 v3, v1 offset:4
	v_readlane_b32 s2, v254, 6
	v_readlane_b32 s3, v254, 7
	v_readlane_b32 s9, v254, 8
	v_mov_b32_e32 v4, 0x1000
	v_mov_b32_e32 v5, 1
	s_lshl_b32 s9, s9, 8
	s_add_u32 s4, s2, s9
	s_addc_u32 s5, s3, 0
	global_atomic_add v4, v4, v5, s[4:5] offset:1024 sc0
	s_waitcnt vmcnt(0) lgkmcnt(0)
	v_readfirstlane_b32 s6, v4
	v_readfirstlane_b32 s7, v2
	v_readfirstlane_b32 s8, v3
	v_mov_b32_e32 v4, 0x3000
	s_nop 3
	s_mul_i32 s9, s7, 8
	s_add_u32 s6, s6, 1
	s_mul_i32 s8, s8, 8
	s_mov_b32 s10, 0
	s_cmp_lg_u32 s6, s9
	s_cbranch_scc1 .Lxb_spin_7
	buffer_wbl2 sc1
	s_waitcnt vmcnt(0)
	global_atomic_add v4, v5, s[2:3] offset:1024

; __device__ __forceinline__ unsigned xb_ld(unsigned* p)              { return __hip_atomic_load(p, __ATOMIC_RELAXED, __HIP_MEMORY_SCOPE_AGENT); }
; __device__ __forceinline__ unsigned xb_add(unsigned* p, unsigned v) { return __hip_atomic_fetch_add(p, v, __ATOMIC_RELAXED, __HIP_MEMORY_SCOPE_AGENT); }
; #define XB_SPIN(cond, bar) do { unsigned _sp = 0; while (cond) { __builtin_amdgcn_s_sleep(1); \
;     if ((++_sp & 255u) == 0u) { if (xb_ld(&(bar)[XB_TMO])) break; if (_sp > XB_SPIN_CAP) { atomicAdd(&(bar)[XB_TMO], 1u); break; } } } } while (0)
; __device__ __forceinline__ void xcd_barrier(const XcdBarrier& b) {
;     ...
;     if (threadIdx.x == 0) {
;         unsigned* bar = b.bar;
;         __builtin_amdgcn_s_waitcnt(0);
;         unsigned nloc = b.st[0], nx = b.st[1];
;         if (nloc == 0u) { xcd_barrier_complete(bar, b.x, nloc, nx); b.st[0] = nloc; b.st[1] = nx; }
;         const unsigned old = xb_add(&bar[XB_XSUB(b.x)], 1u);
;         const unsigned gen = old / nloc;
;         if (old + 1u == (gen + 1u) * nloc) {
;             __builtin_amdgcn_fence(__ATOMIC_RELEASE, "agent");
;             asm volatile("s_waitcnt vmcnt(0)" ::: "memory");
;             const unsigned og = xb_add(&bar[XB_TOP], 1u);
;             const unsigned tg = og / nx;
;             if (og + 1u == (tg + 1u) * nx) xb_add(&bar[XB_TOPGEN], 1u);
;             else XB_SPIN(xb_ld(&bar[XB_TOPGEN]) == tg, bar);
.Lpb8_dend:
	s_waitcnt vmcnt(0)
	s_waitcnt vmcnt(0) lgkmcnt(0)
	s_barrier
	s_mov_b64 s[0:1], exec
	v_readlane_b32 s2, v254, 9
	v_readlane_b32 s3, v254, 10
	s_and_b64 s[2:3], s[0:1], s[2:3]
	s_xor_b64 s[0:1], s[2:3], s[0:1]
	s_mov_b64 exec, s[2:3]
	s_cbranch_execz .LBB0_1152
	s_waitcnt vmcnt(0) expcnt(0) lgkmcnt(0)
	v_mov_b32_e32 v1, 0x21000
	ds_read_b32 v2, v1
	ds_read_b32 v3, v1 offset:4
	v_readlane_b32 s2, v254, 6
	v_readlane_b32 s3, v254, 7
	v_readlane_b32 s9, v254, 8
	v_mov_b32_e32 v4, 0x1000
	v_mov_b32_e32 v5, 1
	s_lshl_b32 s9, s9, 8
	s_add_u32 s4, s2, s9
	s_addc_u32 s5, s3, 0
	global_atomic_add v4, v4, v5, s[4:5] offset:1024 sc0
	s_waitcnt vmcnt(0) lgkmcnt(0)
	v_readfirstlane_b32 s6, v4
	v_readfirstlane_b32 s7, v2
	v_readfirstlane_b32 s8, v3
	v_mov_b32_e32 v4, 0x3000
	s_nop 3
	s_mul_i32 s9, s7, 9
	s_add_u32 s6, s6, 1
	s_mul_i32 s8, s8, 9
	s_mov_b32 s10, 0
	s_cmp_lg_u32 s6, s9
	s_cbranch_scc1 .Lxb_spin_8
	buffer_wbl2 sc1
	s_waitcnt vmcnt(0)
	global_atomic_add v4, v5, s[2:3] offset:1024

; __device__ __forceinline__ unsigned xb_ld(unsigned* p)              { return __hip_atomic_load(p, __ATOMIC_RELAXED, __HIP_MEMORY_SCOPE_AGENT); }
; __device__ __forceinline__ unsigned xb_add(unsigned* p, unsigned v) { return __hip_atomic_fetch_add(p, v, __ATOMIC_RELAXED, __HIP_MEMORY_SCOPE_AGENT); }
; #define XB_SPIN(cond, bar) do { unsigned _sp = 0; while (cond) { __builtin_amdgcn_s_sleep(1); \
;     if ((++_sp & 255u) == 0u) { if (xb_ld(&(bar)[XB_TMO])) break; if (_sp > XB_SPIN_CAP) { atomicAdd(&(bar)[XB_TMO], 1u); break; } } } } while (0)
; __device__ __forceinline__ void xcd_barrier(const XcdBarrier& b) {
;     ...
;     if (threadIdx.x == 0) {
;         unsigned* bar = b.bar;
;         __builtin_amdgcn_s_waitcnt(0);
;         unsigned nloc = b.st[0], nx = b.st[1];
;         if (nloc == 0u) { xcd_barrier_complete(bar, b.x, nloc, nx); b.st[0] = nloc; b.st[1] = nx; }
;         const unsigned old = xb_add(&bar[XB_XSUB(b.x)], 1u);
;         const unsigned gen = old / nloc;
;         if (old + 1u == (gen + 1u) * nloc) {
;             __builtin_amdgcn_fence(__ATOMIC_RELEASE, "agent");
;             asm volatile("s_waitcnt vmcnt(0)" ::: "memory");
;             const unsigned og = xb_add(&bar[XB_TOP], 1u);
;             const unsigned tg = og / nx;
;             if (og + 1u == (tg + 1u) * nx) xb_add(&bar[XB_TOPGEN], 1u);
;             else XB_SPIN(xb_ld(&bar[XB_TOPGEN]) == tg, bar);
.Lpb9_dend:
	s_waitcnt vmcnt(0)
	s_waitcnt vmcnt(0) lgkmcnt(0)
	s_barrier
	s_mov_b64 s[0:1], exec
	v_readlane_b32 s2, v254, 9
	v_readlane_b32 s3, v254, 10
	s_and_b64 s[2:3], s[0:1], s[2:3]
	s_xor_b64 s[0:1], s[2:3], s[0:1]
	s_mov_b64 exec, s[2:3]
	s_cbranch_execz .LBB0_1219
	s_waitcnt vmcnt(0) expcnt(0) lgkmcnt(0)
	v_mov_b32_e32 v1, 0x21000
	ds_read_b32 v2, v1
	ds_read_b32 v3, v1 offset:4
	v_readlane_b32 s2, v254, 6
	v_readlane_b32 s3, v254, 7
	v_readlane_b32 s9, v254, 8
	v_mov_b32_e32 v4, 0x1000
	v_mov_b32_e32 v5, 1
	s_lshl_b32 s9, s9, 8
	s_add_u32 s4, s2, s9
	s_addc_u32 s5, s3, 0
	global_atomic_add v4, v4, v5, s[4:5] offset:1024 sc0
	s_waitcnt vmcnt(0) lgkmcnt(0)
	v_readfirstlane_b32 s6, v4
	v_readfirstlane_b32 s7, v2
	v_readfirstlane_b32 s8, v3
	v_mov_b32_e32 v4, 0x3000
	s_nop 3
	s_mul_i32 s9, s7, 10
	s_add_u32 s6, s6, 1
	s_mul_i32 s8, s8, 10
	s_mov_b32 s10, 0
	s_cmp_lg_u32 s6, s9
	s_cbranch_scc1 .Lxb_spin_9
	buffer_wbl2 sc1
	s_waitcnt vmcnt(0)
	global_atomic_add v4, v5, s[2:3] offset:1024

; __device__ __forceinline__ unsigned xb_ld(unsigned* p)              { return __hip_atomic_load(p, __ATOMIC_RELAXED, __HIP_MEMORY_SCOPE_AGENT); }
; __device__ __forceinline__ unsigned xb_add(unsigned* p, unsigned v) { return __hip_atomic_fetch_add(p, v, __ATOMIC_RELAXED, __HIP_MEMORY_SCOPE_AGENT); }
; #define XB_SPIN(cond, bar) do { unsigned _sp = 0; while (cond) { __builtin_amdgcn_s_sleep(1); \
;     if ((++_sp & 255u) == 0u) { if (xb_ld(&(bar)[XB_TMO])) break; if (_sp > XB_SPIN_CAP) { atomicAdd(&(bar)[XB_TMO], 1u); break; } } } } while (0)
; __device__ __forceinline__ void xcd_barrier(const XcdBarrier& b) {
;     ...
;     if (threadIdx.x == 0) {
;         unsigned* bar = b.bar;
;         __builtin_amdgcn_s_waitcnt(0);
;         unsigned nloc = b.st[0], nx = b.st[1];
;         if (nloc == 0u) { xcd_barrier_complete(bar, b.x, nloc, nx); b.st[0] = nloc; b.st[1] = nx; }
;         const unsigned old = xb_add(&bar[XB_XSUB(b.x)], 1u);
;         const unsigned gen = old / nloc;
;         if (old + 1u == (gen + 1u) * nloc) {
;             __builtin_amdgcn_fence(__ATOMIC_RELEASE, "agent");
;             asm volatile("s_waitcnt vmcnt(0)" ::: "memory");
;             const unsigned og = xb_add(&bar[XB_TOP], 1u);
;             const unsigned tg = og / nx;
;             if (og + 1u == (tg + 1u) * nx) xb_add(&bar[XB_TOPGEN], 1u);
;             else XB_SPIN(xb_ld(&bar[XB_TOPGEN]) == tg, bar);
;             __builtin_amdgcn_fence(__ATOMIC_ACQUIRE, "agent");
;             xb_add(&bar[XB_XGEN(b.x)], 1u);
;             asm volatile("s_waitcnt vmcnt(0)" ::: "memory");
;         } else {
;             XB_SPIN(xb_ld(&bar[XB_XGEN(b.x)]) == gen, bar);
.LBB0_1229:
	s_barrier
	s_waitcnt vmcnt(0)
	s_barrier
	s_mov_b64 s[0:1], exec
	v_readlane_b32 s2, v254, 9
	v_readlane_b32 s3, v254, 10
	s_and_b64 s[2:3], s[0:1], s[2:3]
	s_mov_b64 exec, s[2:3]
	s_cbranch_execz .LBB0_1281
	s_waitcnt vmcnt(0) expcnt(0) lgkmcnt(0)
	v_mov_b32_e32 v1, 0x21000
	ds_read_b32 v2, v1
	ds_read_b32 v3, v1 offset:4
	v_readlane_b32 s2, v254, 6
	v_readlane_b32 s3, v254, 7
	v_readlane_b32 s11, v254, 8
	v_mov_b32_e32 v4, 0x1000
	v_mov_b32_e32 v5, 1
	s_lshl_b32 s11, s11, 8
	s_add_u32 s4, s2, s11
	s_addc_u32 s5, s3, 0
	global_atomic_add v4, v4, v5, s[4:5] offset:1024 sc0
	s_waitcnt vmcnt(0) lgkmcnt(0)
	v_readfirstlane_b32 s6, v4
	v_readfirstlane_b32 s7, v2
	v_readfirstlane_b32 s10, v3
	v_mov_b32_e32 v4, 0x3000
	s_nop 3
	s_mul_i32 s11, s7, 11
	s_add_u32 s6, s6, 1
	s_mul_i32 s10, s10, 11
	s_mov_b32 s12, 0
	s_cmp_lg_u32 s6, s11
	s_cbranch_scc1 .Lxb_spin_10
	buffer_wbl2 sc1
	s_waitcnt vmcnt(0)
	global_atomic_add v4, v5, s[2:3] offset:1024
.Lxb_spin_10:
	global_load_dword v1, v4, s[2:3] offset:1024 sc1
	s_waitcnt vmcnt(0)
	v_readfirstlane_b32 s11, v1
	s_nop 3
	s_cmp_ge_u32 s11, s10
	s_cbranch_scc1 .Lxb_done_10
	s_sleep 1
	s_add_u32 s12, s12, 1
	s_cmp_lt_u32 s12, 0x20000
	s_cbranch_scc1 .Lxb_spin_10

; __device__ __forceinline__ unsigned xb_ld(unsigned* p)              { return __hip_atomic_load(p, __ATOMIC_RELAXED, __HIP_MEMORY_SCOPE_AGENT); }
; __device__ __forceinline__ unsigned xb_add(unsigned* p, unsigned v) { return __hip_atomic_fetch_add(p, v, __ATOMIC_RELAXED, __HIP_MEMORY_SCOPE_AGENT); }
; #define XB_SPIN(cond, bar) do { unsigned _sp = 0; while (cond) { __builtin_amdgcn_s_sleep(1); \
;     if ((++_sp & 255u) == 0u) { if (xb_ld(&(bar)[XB_TMO])) break; if (_sp > XB_SPIN_CAP) { atomicAdd(&(bar)[XB_TMO], 1u); break; } } } } while (0)
; __device__ __forceinline__ void xcd_barrier(const XcdBarrier& b) {
;     ...
;     if (threadIdx.x == 0) {
;         unsigned* bar = b.bar;
;         __builtin_amdgcn_s_waitcnt(0);
;         unsigned nloc = b.st[0], nx = b.st[1];
;         if (nloc == 0u) { xcd_barrier_complete(bar, b.x, nloc, nx); b.st[0] = nloc; b.st[1] = nx; }
;         const unsigned old = xb_add(&bar[XB_XSUB(b.x)], 1u);
;         const unsigned gen = old / nloc;
;         if (old + 1u == (gen + 1u) * nloc) {
;             __builtin_amdgcn_fence(__ATOMIC_RELEASE, "agent");
;             asm volatile("s_waitcnt vmcnt(0)" ::: "memory");
;             const unsigned og = xb_add(&bar[XB_TOP], 1u);
;             const unsigned tg = og / nx;
;             if (og + 1u == (tg + 1u) * nx) xb_add(&bar[XB_TOPGEN], 1u);
;             else XB_SPIN(xb_ld(&bar[XB_TOPGEN]) == tg, bar);
.LBB0_1295:
	s_waitcnt vmcnt(0)
	s_waitcnt vmcnt(0) lgkmcnt(0)
	s_barrier
	s_mov_b64 s[0:1], exec
	v_readlane_b32 s2, v254, 9
	v_readlane_b32 s3, v254, 10
	s_and_b64 s[2:3], s[0:1], s[2:3]
	s_xor_b64 s[0:1], s[2:3], s[0:1]
	s_mov_b64 exec, s[2:3]
	s_cbranch_execz .LBB0_1348
	s_waitcnt vmcnt(0) expcnt(0) lgkmcnt(0)
	v_mov_b32_e32 v1, 0x21000
	ds_read_b32 v2, v1
	ds_read_b32 v3, v1 offset:4
	v_readlane_b32 s2, v254, 6
	v_readlane_b32 s3, v254, 7
	v_readlane_b32 s11, v254, 8
	v_mov_b32_e32 v4, 0x1000
	v_mov_b32_e32 v5, 1
	s_lshl_b32 s11, s11, 8
	s_add_u32 s4, s2, s11
	s_addc_u32 s5, s3, 0
	global_atomic_add v4, v4, v5, s[4:5] offset:1024 sc0
	s_waitcnt vmcnt(0) lgkmcnt(0)
	v_readfirstlane_b32 s6, v4
	v_readfirstlane_b32 s7, v2
	v_readfirstlane_b32 s10, v3
	v_mov_b32_e32 v4, 0x3000
	s_nop 3
	s_mul_i32 s11, s7, 12
	s_add_u32 s6, s6, 1
	s_mul_i32 s10, s10, 12
	s_mov_b32 s12, 0
	s_cmp_lg_u32 s6, s11
	s_cbranch_scc1 .Lxb_spin_11
	buffer_wbl2 sc1
	s_waitcnt vmcnt(0)
	global_atomic_add v4, v5, s[2:3] offset:1024

; __device__ __forceinline__ unsigned xb_ld(unsigned* p)              { return __hip_atomic_load(p, __ATOMIC_RELAXED, __HIP_MEMORY_SCOPE_AGENT); }
; __device__ __forceinline__ unsigned xb_add(unsigned* p, unsigned v) { return __hip_atomic_fetch_add(p, v, __ATOMIC_RELAXED, __HIP_MEMORY_SCOPE_AGENT); }
; #define XB_SPIN(cond, bar) do { unsigned _sp = 0; while (cond) { __builtin_amdgcn_s_sleep(1); \
;     if ((++_sp & 255u) == 0u) { if (xb_ld(&(bar)[XB_TMO])) break; if (_sp > XB_SPIN_CAP) { atomicAdd(&(bar)[XB_TMO], 1u); break; } } } } while (0)
; __device__ __forceinline__ void xcd_barrier(const XcdBarrier& b) {
;     ...
;     if (threadIdx.x == 0) {
;         unsigned* bar = b.bar;
;         __builtin_amdgcn_s_waitcnt(0);
;         unsigned nloc = b.st[0], nx = b.st[1];
;         if (nloc == 0u) { xcd_barrier_complete(bar, b.x, nloc, nx); b.st[0] = nloc; b.st[1] = nx; }
;         const unsigned old = xb_add(&bar[XB_XSUB(b.x)], 1u);
;         const unsigned gen = old / nloc;
;         if (old + 1u == (gen + 1u) * nloc) {
;             __builtin_amdgcn_fence(__ATOMIC_RELEASE, "agent");
;             asm volatile("s_waitcnt vmcnt(0)" ::: "memory");
;             const unsigned og = xb_add(&bar[XB_TOP], 1u);
;             const unsigned tg = og / nx;
;             if (og + 1u == (tg + 1u) * nx) xb_add(&bar[XB_TOPGEN], 1u);
;             else XB_SPIN(xb_ld(&bar[XB_TOPGEN]) == tg, bar);
.LBB0_1389:
	s_barrier
	s_waitcnt vmcnt(0)
	s_barrier
	s_mov_b64 s[0:1], exec
	v_readlane_b32 s2, v254, 9
	v_readlane_b32 s3, v254, 10
	s_and_b64 s[2:3], s[0:1], s[2:3]
	s_mov_b64 exec, s[2:3]
	s_cbranch_execz .LBB0_1441
	s_waitcnt vmcnt(0) expcnt(0) lgkmcnt(0)
	v_mov_b32_e32 v1, 0x21000
	ds_read_b32 v2, v1
	ds_read_b32 v3, v1 offset:4
	v_readlane_b32 s2, v254, 6
	v_readlane_b32 s3, v254, 7
	v_readlane_b32 s11, v254, 8
	v_mov_b32_e32 v4, 0x1000
	v_mov_b32_e32 v5, 1
	s_lshl_b32 s11, s11, 8
	s_add_u32 s4, s2, s11
	s_addc_u32 s5, s3, 0
	global_atomic_add v4, v4, v5, s[4:5] offset:1024 sc0
	s_waitcnt vmcnt(0) lgkmcnt(0)
	v_readfirstlane_b32 s6, v4
	v_readfirstlane_b32 s7, v2
	v_readfirstlane_b32 s10, v3
	v_mov_b32_e32 v4, 0x3000
	s_nop 3
	s_mul_i32 s11, s7, 13
	s_add_u32 s6, s6, 1
	s_mul_i32 s10, s10, 13
	s_mov_b32 s12, 0
	s_cmp_lg_u32 s6, s11
	s_cbranch_scc1 .Lxb_spin_12
	buffer_wbl2 sc1
	s_waitcnt vmcnt(0)
	global_atomic_add v4, v5, s[2:3] offset:1024

; __device__ __forceinline__ unsigned xb_ld(unsigned* p)              { return __hip_atomic_load(p, __ATOMIC_RELAXED, __HIP_MEMORY_SCOPE_AGENT); }
; __device__ __forceinline__ unsigned xb_add(unsigned* p, unsigned v) { return __hip_atomic_fetch_add(p, v, __ATOMIC_RELAXED, __HIP_MEMORY_SCOPE_AGENT); }
; #define XB_SPIN(cond, bar) do { unsigned _sp = 0; while (cond) { __builtin_amdgcn_s_sleep(1); \
;     if ((++_sp & 255u) == 0u) { if (xb_ld(&(bar)[XB_TMO])) break; if (_sp > XB_SPIN_CAP) { atomicAdd(&(bar)[XB_TMO], 1u); break; } } } } while (0)
; __device__ __forceinline__ void xcd_barrier(const XcdBarrier& b) {
;     ...
;     if (threadIdx.x == 0) {
;         unsigned* bar = b.bar;
;         __builtin_amdgcn_s_waitcnt(0);
;         unsigned nloc = b.st[0], nx = b.st[1];
;         if (nloc == 0u) { xcd_barrier_complete(bar, b.x, nloc, nx); b.st[0] = nloc; b.st[1] = nx; }
;         const unsigned old = xb_add(&bar[XB_XSUB(b.x)], 1u);
;         const unsigned gen = old / nloc;
;         if (old + 1u == (gen + 1u) * nloc) {
;             __builtin_amdgcn_fence(__ATOMIC_RELEASE, "agent");
;             asm volatile("s_waitcnt vmcnt(0)" ::: "memory");
;             const unsigned og = xb_add(&bar[XB_TOP], 1u);
;             const unsigned tg = og / nx;
;             if (og + 1u == (tg + 1u) * nx) xb_add(&bar[XB_TOPGEN], 1u);
;             else XB_SPIN(xb_ld(&bar[XB_TOPGEN]) == tg, bar);
.LBB0_1447:
	s_or_b64 exec, exec, s[2:3]
	s_waitcnt vmcnt(0)
	s_barrier
	s_mov_b64 s[0:1], exec
	v_readlane_b32 s2, v254, 9
	v_readlane_b32 s3, v254, 10
	s_and_b64 s[2:3], s[0:1], s[2:3]
	s_mov_b64 exec, s[2:3]
	s_cbranch_execz .LBB0_1499
	s_waitcnt vmcnt(0) expcnt(0) lgkmcnt(0)
	v_mov_b32_e32 v1, 0x21000
	ds_read_b32 v2, v1
	ds_read_b32 v3, v1 offset:4
	v_readlane_b32 s2, v254, 6
	v_readlane_b32 s3, v254, 7
	v_readlane_b32 s11, v254, 8
	v_mov_b32_e32 v4, 0x1000
	v_mov_b32_e32 v5, 1
	s_lshl_b32 s11, s11, 8
	s_add_u32 s4, s2, s11
	s_addc_u32 s5, s3, 0
	global_atomic_add v4, v4, v5, s[4:5] offset:1024 sc0
	s_waitcnt vmcnt(0) lgkmcnt(0)
	v_readfirstlane_b32 s6, v4
	v_readfirstlane_b32 s7, v2
	v_readfirstlane_b32 s10, v3
	v_mov_b32_e32 v4, 0x3000
	s_nop 3
	s_mul_i32 s11, s7, 14
	s_add_u32 s6, s6, 1
	s_mul_i32 s10, s10, 14
	s_mov_b32 s12, 0
	s_cmp_lg_u32 s6, s11
	s_cbranch_scc1 .Lxb_spin_13
	buffer_wbl2 sc1
	s_waitcnt vmcnt(0)
	global_atomic_add v4, v5, s[2:3] offset:1024

; __device__ __forceinline__ unsigned xb_ld(unsigned* p)              { return __hip_atomic_load(p, __ATOMIC_RELAXED, __HIP_MEMORY_SCOPE_AGENT); }
; __device__ __forceinline__ unsigned xb_add(unsigned* p, unsigned v) { return __hip_atomic_fetch_add(p, v, __ATOMIC_RELAXED, __HIP_MEMORY_SCOPE_AGENT); }
; #define XB_SPIN(cond, bar) do { unsigned _sp = 0; while (cond) { __builtin_amdgcn_s_sleep(1); \
;     if ((++_sp & 255u) == 0u) { if (xb_ld(&(bar)[XB_TMO])) break; if (_sp > XB_SPIN_CAP) { atomicAdd(&(bar)[XB_TMO], 1u); break; } } } } while (0)
; __device__ __forceinline__ void xcd_barrier(const XcdBarrier& b) {
;     ...
;     if (threadIdx.x == 0) {
;         unsigned* bar = b.bar;
;         __builtin_amdgcn_s_waitcnt(0);
;         unsigned nloc = b.st[0], nx = b.st[1];
;         if (nloc == 0u) { xcd_barrier_complete(bar, b.x, nloc, nx); b.st[0] = nloc; b.st[1] = nx; }
;         const unsigned old = xb_add(&bar[XB_XSUB(b.x)], 1u);
;         const unsigned gen = old / nloc;
;         if (old + 1u == (gen + 1u) * nloc) {
;             __builtin_amdgcn_fence(__ATOMIC_RELEASE, "agent");
;             asm volatile("s_waitcnt vmcnt(0)" ::: "memory");
;             const unsigned og = xb_add(&bar[XB_TOP], 1u);
;             const unsigned tg = og / nx;
;             if (og + 1u == (tg + 1u) * nx) xb_add(&bar[XB_TOPGEN], 1u);
;             else XB_SPIN(xb_ld(&bar[XB_TOPGEN]) == tg, bar);
.LBB0_1614:
	s_barrier
	s_waitcnt vmcnt(0)
	s_barrier
	s_mov_b64 s[0:1], exec
	v_readlane_b32 s2, v254, 9
	v_readlane_b32 s3, v254, 10
	s_and_b64 s[2:3], s[0:1], s[2:3]
	s_mov_b64 exec, s[2:3]
	s_cbranch_execz .LBB0_1666
	s_waitcnt vmcnt(0) expcnt(0) lgkmcnt(0)
	v_mov_b32_e32 v1, 0x21000
	ds_read_b32 v2, v1
	ds_read_b32 v3, v1 offset:4
	v_readlane_b32 s2, v254, 6
	v_readlane_b32 s3, v254, 7
	v_readlane_b32 s11, v254, 8
	v_mov_b32_e32 v4, 0x1000
	v_mov_b32_e32 v5, 1
	s_lshl_b32 s11, s11, 8
	s_add_u32 s4, s2, s11
	s_addc_u32 s5, s3, 0
	global_atomic_add v4, v4, v5, s[4:5] offset:1024 sc0
	s_waitcnt vmcnt(0) lgkmcnt(0)
	v_readfirstlane_b32 s6, v4
	v_readfirstlane_b32 s7, v2
	v_readfirstlane_b32 s10, v3
	v_mov_b32_e32 v4, 0x3000
	s_nop 3
	s_mul_i32 s11, s7, 15
	s_add_u32 s6, s6, 1
	s_mul_i32 s10, s10, 15
	s_mov_b32 s12, 0
	s_cmp_lg_u32 s6, s11
	s_cbranch_scc1 .Lxb_spin_14
	buffer_wbl2 sc1
	s_waitcnt vmcnt(0)
	global_atomic_add v4, v5, s[2:3] offset:1024

; __device__ __forceinline__ unsigned xb_ld(unsigned* p)              { return __hip_atomic_load(p, __ATOMIC_RELAXED, __HIP_MEMORY_SCOPE_AGENT); }
; __device__ __forceinline__ unsigned xb_add(unsigned* p, unsigned v) { return __hip_atomic_fetch_add(p, v, __ATOMIC_RELAXED, __HIP_MEMORY_SCOPE_AGENT); }
; #define XB_SPIN(cond, bar) do { unsigned _sp = 0; while (cond) { __builtin_amdgcn_s_sleep(1); \
;     if ((++_sp & 255u) == 0u) { if (xb_ld(&(bar)[XB_TMO])) break; if (_sp > XB_SPIN_CAP) { atomicAdd(&(bar)[XB_TMO], 1u); break; } } } } while (0)
; __device__ __forceinline__ void xcd_barrier(const XcdBarrier& b) {
;     ...
;     if (threadIdx.x == 0) {
;         unsigned* bar = b.bar;
;         __builtin_amdgcn_s_waitcnt(0);
;         unsigned nloc = b.st[0], nx = b.st[1];
;         if (nloc == 0u) { xcd_barrier_complete(bar, b.x, nloc, nx); b.st[0] = nloc; b.st[1] = nx; }
;         const unsigned old = xb_add(&bar[XB_XSUB(b.x)], 1u);
;         const unsigned gen = old / nloc;
;         if (old + 1u == (gen + 1u) * nloc) {
;             __builtin_amdgcn_fence(__ATOMIC_RELEASE, "agent");
;             asm volatile("s_waitcnt vmcnt(0)" ::: "memory");
;             const unsigned og = xb_add(&bar[XB_TOP], 1u);
;             const unsigned tg = og / nx;
;             if (og + 1u == (tg + 1u) * nx) xb_add(&bar[XB_TOPGEN], 1u);
;             else XB_SPIN(xb_ld(&bar[XB_TOPGEN]) == tg, bar);
.LBB0_1684:
	s_waitcnt vmcnt(0)
	s_waitcnt lgkmcnt(0)
	s_barrier
	s_mov_b64 s[0:1], exec
	v_readlane_b32 s2, v254, 9
	v_readlane_b32 s3, v254, 10
	s_and_b64 s[2:3], s[0:1], s[2:3]
	s_xor_b64 s[0:1], s[2:3], s[0:1]
	s_mov_b64 exec, s[2:3]
	s_cbranch_execz .LBB0_1737
	s_waitcnt vmcnt(0) expcnt(0) lgkmcnt(0)
	v_mov_b32_e32 v1, 0x21000
	ds_read_b32 v2, v1
	ds_read_b32 v3, v1 offset:4
	v_readlane_b32 s2, v254, 6
	v_readlane_b32 s3, v254, 7
	v_readlane_b32 s11, v254, 8
	v_mov_b32_e32 v4, 0x1000
	v_mov_b32_e32 v5, 1
	s_lshl_b32 s11, s11, 8
	s_add_u32 s4, s2, s11
	s_addc_u32 s5, s3, 0
	global_atomic_add v4, v4, v5, s[4:5] offset:1024 sc0
	s_waitcnt vmcnt(0) lgkmcnt(0)
	v_readfirstlane_b32 s6, v4
	v_readfirstlane_b32 s7, v2
	v_readfirstlane_b32 s10, v3
	v_mov_b32_e32 v4, 0x3000
	s_nop 3
	s_mul_i32 s11, s7, 16
	s_add_u32 s6, s6, 1
	s_mul_i32 s10, s10, 16
	s_mov_b32 s12, 0
	s_cmp_lg_u32 s6, s11
	s_cbranch_scc1 .Lxb_spin_15
	buffer_wbl2 sc1
	s_waitcnt vmcnt(0)
	global_atomic_add v4, v5, s[2:3] offset:1024

; __device__ __forceinline__ unsigned xb_ld(unsigned* p)              { return __hip_atomic_load(p, __ATOMIC_RELAXED, __HIP_MEMORY_SCOPE_AGENT); }
; __device__ __forceinline__ unsigned xb_add(unsigned* p, unsigned v) { return __hip_atomic_fetch_add(p, v, __ATOMIC_RELAXED, __HIP_MEMORY_SCOPE_AGENT); }
; #define XB_SPIN(cond, bar) do { unsigned _sp = 0; while (cond) { __builtin_amdgcn_s_sleep(1); \
;     if ((++_sp & 255u) == 0u) { if (xb_ld(&(bar)[XB_TMO])) break; if (_sp > XB_SPIN_CAP) { atomicAdd(&(bar)[XB_TMO], 1u); break; } } } } while (0)
; __device__ __forceinline__ void xcd_barrier(const XcdBarrier& b) {
;     ...
;     if (threadIdx.x == 0) {
;         unsigned* bar = b.bar;
;         __builtin_amdgcn_s_waitcnt(0);
;         unsigned nloc = b.st[0], nx = b.st[1];
;         if (nloc == 0u) { xcd_barrier_complete(bar, b.x, nloc, nx); b.st[0] = nloc; b.st[1] = nx; }
;         const unsigned old = xb_add(&bar[XB_XSUB(b.x)], 1u);
;         const unsigned gen = old / nloc;
;         if (old + 1u == (gen + 1u) * nloc) {
;             __builtin_amdgcn_fence(__ATOMIC_RELEASE, "agent");
;             asm volatile("s_waitcnt vmcnt(0)" ::: "memory");
;             const unsigned og = xb_add(&bar[XB_TOP], 1u);
;             const unsigned tg = og / nx;
;             if (og + 1u == (tg + 1u) * nx) xb_add(&bar[XB_TOPGEN], 1u);
;             else XB_SPIN(xb_ld(&bar[XB_TOPGEN]) == tg, bar);
.LBB0_1746:
	s_waitcnt lgkmcnt(0)
	s_barrier
	s_waitcnt vmcnt(0)
	s_barrier
	s_mov_b64 s[0:1], exec
	v_readlane_b32 s2, v254, 9
	v_readlane_b32 s3, v254, 10
	s_and_b64 s[2:3], s[0:1], s[2:3]
	s_mov_b64 exec, s[2:3]
	s_cbranch_execz .LBB0_1798
	s_waitcnt vmcnt(0) expcnt(0) lgkmcnt(0)
	v_mov_b32_e32 v1, 0x21000
	ds_read_b32 v2, v1
	ds_read_b32 v3, v1 offset:4
	v_readlane_b32 s2, v254, 6
	v_readlane_b32 s3, v254, 7
	v_readlane_b32 s9, v254, 8
	v_mov_b32_e32 v4, 0x1000
	v_mov_b32_e32 v5, 1
	s_lshl_b32 s9, s9, 8
	s_add_u32 s4, s2, s9
	s_addc_u32 s5, s3, 0
	global_atomic_add v4, v4, v5, s[4:5] offset:1024 sc0
	s_waitcnt vmcnt(0) lgkmcnt(0)
	v_readfirstlane_b32 s6, v4
	v_readfirstlane_b32 s7, v2
	v_readfirstlane_b32 s8, v3
	v_mov_b32_e32 v4, 0x3000
	s_nop 3
	s_mul_i32 s9, s7, 17
	s_add_u32 s6, s6, 1
	s_mul_i32 s8, s8, 17
	s_mov_b32 s10, 0
	s_cmp_lg_u32 s6, s9
	s_cbranch_scc1 .Lxb_spin_16
	buffer_wbl2 sc1
	s_waitcnt vmcnt(0)
	global_atomic_add v4, v5, s[2:3] offset:1024

; __device__ __forceinline__ unsigned xb_ld(unsigned* p)              { return __hip_atomic_load(p, __ATOMIC_RELAXED, __HIP_MEMORY_SCOPE_AGENT); }
; __device__ __forceinline__ unsigned xb_add(unsigned* p, unsigned v) { return __hip_atomic_fetch_add(p, v, __ATOMIC_RELAXED, __HIP_MEMORY_SCOPE_AGENT); }
; #define XB_SPIN(cond, bar) do { unsigned _sp = 0; while (cond) { __builtin_amdgcn_s_sleep(1); \
;     if ((++_sp & 255u) == 0u) { if (xb_ld(&(bar)[XB_TMO])) break; if (_sp > XB_SPIN_CAP) { atomicAdd(&(bar)[XB_TMO], 1u); break; } } } } while (0)
; __device__ __forceinline__ void xcd_barrier(const XcdBarrier& b) {
;     ...
;     if (threadIdx.x == 0) {
;         unsigned* bar = b.bar;
;         __builtin_amdgcn_s_waitcnt(0);
;         unsigned nloc = b.st[0], nx = b.st[1];
;         if (nloc == 0u) { xcd_barrier_complete(bar, b.x, nloc, nx); b.st[0] = nloc; b.st[1] = nx; }
;         const unsigned old = xb_add(&bar[XB_XSUB(b.x)], 1u);
;         const unsigned gen = old / nloc;
;         if (old + 1u == (gen + 1u) * nloc) {
;             __builtin_amdgcn_fence(__ATOMIC_RELEASE, "agent");
;             asm volatile("s_waitcnt vmcnt(0)" ::: "memory");
;             const unsigned og = xb_add(&bar[XB_TOP], 1u);
;             const unsigned tg = og / nx;
;             if (og + 1u == (tg + 1u) * nx) xb_add(&bar[XB_TOPGEN], 1u);
;             else XB_SPIN(xb_ld(&bar[XB_TOPGEN]) == tg, bar);
.Lpb17_dend:
	s_waitcnt vmcnt(0)
	s_waitcnt vmcnt(0) lgkmcnt(0)
	s_barrier
	s_mov_b64 s[0:1], exec
	v_readlane_b32 s2, v254, 9
	v_readlane_b32 s3, v254, 10
	s_and_b64 s[2:3], s[0:1], s[2:3]
	s_xor_b64 s[0:1], s[2:3], s[0:1]
	s_mov_b64 exec, s[2:3]
	s_cbranch_execz .LBB0_1889
	s_waitcnt vmcnt(0) expcnt(0) lgkmcnt(0)
	v_mov_b32_e32 v1, 0x21000
	ds_read_b32 v2, v1
	ds_read_b32 v3, v1 offset:4
	v_readlane_b32 s2, v254, 6
	v_readlane_b32 s3, v254, 7
	v_readlane_b32 s9, v254, 8
	v_mov_b32_e32 v4, 0x1000
	v_mov_b32_e32 v5, 1
	s_lshl_b32 s9, s9, 8
	s_add_u32 s4, s2, s9
	s_addc_u32 s5, s3, 0
	global_atomic_add v4, v4, v5, s[4:5] offset:1024 sc0
	s_waitcnt vmcnt(0) lgkmcnt(0)
	v_readfirstlane_b32 s6, v4
	v_readfirstlane_b32 s7, v2
	v_readfirstlane_b32 s8, v3
	v_mov_b32_e32 v4, 0x3000
	s_nop 3
	s_mul_i32 s9, s7, 18
	s_add_u32 s6, s6, 1
	s_mul_i32 s8, s8, 18
	s_mov_b32 s10, 0
	s_cmp_lg_u32 s6, s9
	s_cbranch_scc1 .Lxb_spin_17
	buffer_wbl2 sc1
	s_waitcnt vmcnt(0)
	global_atomic_add v4, v5, s[2:3] offset:1024

; __device__ __forceinline__ unsigned xb_ld(unsigned* p)              { return __hip_atomic_load(p, __ATOMIC_RELAXED, __HIP_MEMORY_SCOPE_AGENT); }
; __device__ __forceinline__ unsigned xb_add(unsigned* p, unsigned v) { return __hip_atomic_fetch_add(p, v, __ATOMIC_RELAXED, __HIP_MEMORY_SCOPE_AGENT); }
; #define XB_SPIN(cond, bar) do { unsigned _sp = 0; while (cond) { __builtin_amdgcn_s_sleep(1); \
;     if ((++_sp & 255u) == 0u) { if (xb_ld(&(bar)[XB_TMO])) break; if (_sp > XB_SPIN_CAP) { atomicAdd(&(bar)[XB_TMO], 1u); break; } } } } while (0)
; __device__ __forceinline__ void xcd_barrier(const XcdBarrier& b) {
;     ...
;     if (threadIdx.x == 0) {
;         unsigned* bar = b.bar;
;         __builtin_amdgcn_s_waitcnt(0);
;         unsigned nloc = b.st[0], nx = b.st[1];
;         if (nloc == 0u) { xcd_barrier_complete(bar, b.x, nloc, nx); b.st[0] = nloc; b.st[1] = nx; }
;         const unsigned old = xb_add(&bar[XB_XSUB(b.x)], 1u);
;         const unsigned gen = old / nloc;
;         if (old + 1u == (gen + 1u) * nloc) {
;             __builtin_amdgcn_fence(__ATOMIC_RELEASE, "agent");
;             asm volatile("s_waitcnt vmcnt(0)" ::: "memory");
;             const unsigned og = xb_add(&bar[XB_TOP], 1u);
;             const unsigned tg = og / nx;
;             if (og + 1u == (tg + 1u) * nx) xb_add(&bar[XB_TOPGEN], 1u);
;             else XB_SPIN(xb_ld(&bar[XB_TOPGEN]) == tg, bar);
.LBB0_1903:
	s_waitcnt vmcnt(0)
	s_waitcnt vmcnt(0) lgkmcnt(0)
	s_barrier
	s_mov_b64 s[0:1], exec
	v_readlane_b32 s2, v254, 9
	v_readlane_b32 s3, v254, 10
	s_and_b64 s[2:3], s[0:1], s[2:3]
	s_xor_b64 s[0:1], s[2:3], s[0:1]
	s_mov_b64 exec, s[2:3]
	s_cbranch_execz .LBB0_1956
	s_waitcnt vmcnt(0) expcnt(0) lgkmcnt(0)
	v_mov_b32_e32 v1, 0x21000
	ds_read_b32 v2, v1
	ds_read_b32 v3, v1 offset:4
	v_readlane_b32 s2, v254, 6
	v_readlane_b32 s3, v254, 7
	v_readlane_b32 s9, v254, 8
	v_mov_b32_e32 v4, 0x1000
	v_mov_b32_e32 v5, 1
	s_lshl_b32 s9, s9, 8
	s_add_u32 s4, s2, s9
	s_addc_u32 s5, s3, 0
	global_atomic_add v4, v4, v5, s[4:5] offset:1024 sc0
	s_waitcnt vmcnt(0) lgkmcnt(0)
	v_readfirstlane_b32 s6, v4
	v_readfirstlane_b32 s7, v2
	v_readfirstlane_b32 s8, v3
	v_mov_b32_e32 v4, 0x3000
	s_nop 3
	s_mul_i32 s9, s7, 19
	s_add_u32 s6, s6, 1
	s_mul_i32 s8, s8, 19
	s_mov_b32 s10, 0
	s_cmp_lg_u32 s6, s9
	s_cbranch_scc1 .Lxb_spin_18
	buffer_wbl2 sc1
	s_waitcnt vmcnt(0)
	global_atomic_add v4, v5, s[2:3] offset:1024
